# adaLN phase prologue: silu(c) staging loop de-serialised (16 loads in flight instead of a load-wait per iteration)
# baseline (speedup 1.0000x reference)
; __device__ __forceinline__ void phase0(Frame& F, const Args& a) {
;     ...
;         for (int i = F.tid; i < BATCH * D; i += NWAVES * 64) { const float v = a.c[i]; sl[i] = v / (1.0f + __expf(-v)); }
.LBB0_15:
	global_load_dword v200, v[2:3], off
	v_lshl_add_u64 v[2:3], v[2:3], 0, s[4:5]
	global_load_dword v201, v[2:3], off
	v_lshl_add_u64 v[2:3], v[2:3], 0, s[4:5]
	global_load_dword v202, v[2:3], off
	v_lshl_add_u64 v[2:3], v[2:3], 0, s[4:5]
	global_load_dword v203, v[2:3], off
	v_lshl_add_u64 v[2:3], v[2:3], 0, s[4:5]
	global_load_dword v204, v[2:3], off
	v_lshl_add_u64 v[2:3], v[2:3], 0, s[4:5]
	global_load_dword v205, v[2:3], off
	v_lshl_add_u64 v[2:3], v[2:3], 0, s[4:5]
	global_load_dword v206, v[2:3], off
	v_lshl_add_u64 v[2:3], v[2:3], 0, s[4:5]
	global_load_dword v207, v[2:3], off
	v_lshl_add_u64 v[2:3], v[2:3], 0, s[4:5]
	global_load_dword v208, v[2:3], off
	v_lshl_add_u64 v[2:3], v[2:3], 0, s[4:5]
	global_load_dword v209, v[2:3], off
	v_lshl_add_u64 v[2:3], v[2:3], 0, s[4:5]
	global_load_dword v210, v[2:3], off
	v_lshl_add_u64 v[2:3], v[2:3], 0, s[4:5]
	global_load_dword v211, v[2:3], off
	v_lshl_add_u64 v[2:3], v[2:3], 0, s[4:5]
	global_load_dword v212, v[2:3], off
	v_lshl_add_u64 v[2:3], v[2:3], 0, s[4:5]
	global_load_dword v213, v[2:3], off
	v_lshl_add_u64 v[2:3], v[2:3], 0, s[4:5]
	global_load_dword v214, v[2:3], off
	v_lshl_add_u64 v[2:3], v[2:3], 0, s[4:5]
	global_load_dword v215, v[2:3], off
	v_lshl_add_u64 v[2:3], v[2:3], 0, s[4:5]
	s_waitcnt vmcnt(15)
	v_mul_f32_e32 v7, 0xbfb8aa3b, v200
	v_exp_f32_e32 v7, v7
	s_nop 0
	v_add_f32_e32 v7, 1.0, v7
	v_div_scale_f32 v8, s[8:9], v7, v7, v200
	v_rcp_f32_e32 v9, v8
	v_div_scale_f32 v10, vcc, v200, v7, v200
	v_fma_f32 v11, -v8, v9, 1.0
	v_fmac_f32_e32 v9, v11, v9
	v_mul_f32_e32 v11, v10, v9
	v_fma_f32 v12, -v8, v11, v10
	v_fmac_f32_e32 v11, v12, v9
	v_fma_f32 v8, -v8, v11, v10
	v_div_fmas_f32 v8, v8, v9, v11
	v_div_fixup_f32 v6, v8, v7, v200
	ds_write_b32 v5, v6
	v_add_u32_e32 v5, 0x800, v5
	s_waitcnt vmcnt(14)
	v_mul_f32_e32 v7, 0xbfb8aa3b, v201
	v_exp_f32_e32 v7, v7
	s_nop 0
	v_add_f32_e32 v7, 1.0, v7
	v_div_scale_f32 v8, s[8:9], v7, v7, v201
	v_rcp_f32_e32 v9, v8
	v_div_scale_f32 v10, vcc, v201, v7, v201
	v_fma_f32 v11, -v8, v9, 1.0
	v_fmac_f32_e32 v9, v11, v9
	v_mul_f32_e32 v11, v10, v9
	v_fma_f32 v12, -v8, v11, v10
	v_fmac_f32_e32 v11, v12, v9
	v_fma_f32 v8, -v8, v11, v10
	v_div_fmas_f32 v8, v8, v9, v11
	v_div_fixup_f32 v6, v8, v7, v201
	ds_write_b32 v5, v6
	v_add_u32_e32 v5, 0x800, v5
	s_waitcnt vmcnt(13)
	v_mul_f32_e32 v7, 0xbfb8aa3b, v202
	v_exp_f32_e32 v7, v7
	s_nop 0
	v_add_f32_e32 v7, 1.0, v7
	v_div_scale_f32 v8, s[8:9], v7, v7, v202
	v_rcp_f32_e32 v9, v8
	v_div_scale_f32 v10, vcc, v202, v7, v202
	v_fma_f32 v11, -v8, v9, 1.0
	v_fmac_f32_e32 v9, v11, v9
	v_mul_f32_e32 v11, v10, v9
	v_fma_f32 v12, -v8, v11, v10
	v_fmac_f32_e32 v11, v12, v9
	v_fma_f32 v8, -v8, v11, v10
	v_div_fmas_f32 v8, v8, v9, v11
	v_div_fixup_f32 v6, v8, v7, v202
	ds_write_b32 v5, v6
	v_add_u32_e32 v5, 0x800, v5
	s_waitcnt vmcnt(12)
	v_mul_f32_e32 v7, 0xbfb8aa3b, v203
	v_exp_f32_e32 v7, v7
	s_nop 0
	v_add_f32_e32 v7, 1.0, v7
	v_div_scale_f32 v8, s[8:9], v7, v7, v203
	v_rcp_f32_e32 v9, v8
	v_div_scale_f32 v10, vcc, v203, v7, v203
	v_fma_f32 v11, -v8, v9, 1.0
	v_fmac_f32_e32 v9, v11, v9
	v_mul_f32_e32 v11, v10, v9
	v_fma_f32 v12, -v8, v11, v10
	v_fmac_f32_e32 v11, v12, v9
	v_fma_f32 v8, -v8, v11, v10
	v_div_fmas_f32 v8, v8, v9, v11
	v_div_fixup_f32 v6, v8, v7, v203
	ds_write_b32 v5, v6
	v_add_u32_e32 v5, 0x800, v5
	s_waitcnt vmcnt(11)
	v_mul_f32_e32 v7, 0xbfb8aa3b, v204
	v_exp_f32_e32 v7, v7
	s_nop 0
	v_add_f32_e32 v7, 1.0, v7
	v_div_scale_f32 v8, s[8:9], v7, v7, v204
	v_rcp_f32_e32 v9, v8
	v_div_scale_f32 v10, vcc, v204, v7, v204
	v_fma_f32 v11, -v8, v9, 1.0
	v_fmac_f32_e32 v9, v11, v9
	v_mul_f32_e32 v11, v10, v9
	v_fma_f32 v12, -v8, v11, v10
	v_fmac_f32_e32 v11, v12, v9
	v_fma_f32 v8, -v8, v11, v10
	v_div_fmas_f32 v8, v8, v9, v11
	v_div_fixup_f32 v6, v8, v7, v204
	ds_write_b32 v5, v6
	v_add_u32_e32 v5, 0x800, v5
	s_waitcnt vmcnt(10)
	v_mul_f32_e32 v7, 0xbfb8aa3b, v205
	v_exp_f32_e32 v7, v7
	s_nop 0
	v_add_f32_e32 v7, 1.0, v7
	v_div_scale_f32 v8, s[8:9], v7, v7, v205
	v_rcp_f32_e32 v9, v8
	v_div_scale_f32 v10, vcc, v205, v7, v205
	v_fma_f32 v11, -v8, v9, 1.0
	v_fmac_f32_e32 v9, v11, v9
	v_mul_f32_e32 v11, v10, v9
	v_fma_f32 v12, -v8, v11, v10
	v_fmac_f32_e32 v11, v12, v9
	v_fma_f32 v8, -v8, v11, v10
	v_div_fmas_f32 v8, v8, v9, v11
	v_div_fixup_f32 v6, v8, v7, v205
	ds_write_b32 v5, v6
	v_add_u32_e32 v5, 0x800, v5
	s_waitcnt vmcnt(9)
	v_mul_f32_e32 v7, 0xbfb8aa3b, v206
	v_exp_f32_e32 v7, v7
	s_nop 0
	v_add_f32_e32 v7, 1.0, v7
	v_div_scale_f32 v8, s[8:9], v7, v7, v206
	v_rcp_f32_e32 v9, v8
	v_div_scale_f32 v10, vcc, v206, v7, v206
	v_fma_f32 v11, -v8, v9, 1.0
	v_fmac_f32_e32 v9, v11, v9
	v_mul_f32_e32 v11, v10, v9
	v_fma_f32 v12, -v8, v11, v10
	v_fmac_f32_e32 v11, v12, v9
	v_fma_f32 v8, -v8, v11, v10
	v_div_fmas_f32 v8, v8, v9, v11
	v_div_fixup_f32 v6, v8, v7, v206
	ds_write_b32 v5, v6
	v_add_u32_e32 v5, 0x800, v5
	s_waitcnt vmcnt(8)
; __device__ __forceinline__ void phase0(Frame& F, const Args& a) {
;     ...
;         for (int i = F.tid; i < BATCH * D; i += NWAVES * 64) { const float v = a.c[i]; sl[i] = v / (1.0f + __expf(-v)); }
	v_mul_f32_e32 v7, 0xbfb8aa3b, v207
	v_exp_f32_e32 v7, v7
	s_nop 0
	v_add_f32_e32 v7, 1.0, v7
	v_div_scale_f32 v8, s[8:9], v7, v7, v207
	v_rcp_f32_e32 v9, v8
	v_div_scale_f32 v10, vcc, v207, v7, v207
	v_fma_f32 v11, -v8, v9, 1.0
	v_fmac_f32_e32 v9, v11, v9
	v_mul_f32_e32 v11, v10, v9
	v_fma_f32 v12, -v8, v11, v10
	v_fmac_f32_e32 v11, v12, v9
	v_fma_f32 v8, -v8, v11, v10
	v_div_fmas_f32 v8, v8, v9, v11
	v_div_fixup_f32 v6, v8, v7, v207
	ds_write_b32 v5, v6
	v_add_u32_e32 v5, 0x800, v5
	s_waitcnt vmcnt(7)
	v_mul_f32_e32 v7, 0xbfb8aa3b, v208
	v_exp_f32_e32 v7, v7
	s_nop 0
	v_add_f32_e32 v7, 1.0, v7
	v_div_scale_f32 v8, s[8:9], v7, v7, v208
	v_rcp_f32_e32 v9, v8
	v_div_scale_f32 v10, vcc, v208, v7, v208
	v_fma_f32 v11, -v8, v9, 1.0
	v_fmac_f32_e32 v9, v11, v9
	v_mul_f32_e32 v11, v10, v9
	v_fma_f32 v12, -v8, v11, v10
	v_fmac_f32_e32 v11, v12, v9
	v_fma_f32 v8, -v8, v11, v10
	v_div_fmas_f32 v8, v8, v9, v11
	v_div_fixup_f32 v6, v8, v7, v208
	ds_write_b32 v5, v6
	v_add_u32_e32 v5, 0x800, v5
	s_waitcnt vmcnt(6)
	v_mul_f32_e32 v7, 0xbfb8aa3b, v209
	v_exp_f32_e32 v7, v7
	s_nop 0
	v_add_f32_e32 v7, 1.0, v7
	v_div_scale_f32 v8, s[8:9], v7, v7, v209
	v_rcp_f32_e32 v9, v8
	v_div_scale_f32 v10, vcc, v209, v7, v209
	v_fma_f32 v11, -v8, v9, 1.0
	v_fmac_f32_e32 v9, v11, v9
	v_mul_f32_e32 v11, v10, v9
	v_fma_f32 v12, -v8, v11, v10
	v_fmac_f32_e32 v11, v12, v9
	v_fma_f32 v8, -v8, v11, v10
	v_div_fmas_f32 v8, v8, v9, v11
	v_div_fixup_f32 v6, v8, v7, v209
	ds_write_b32 v5, v6
	v_add_u32_e32 v5, 0x800, v5
	s_waitcnt vmcnt(5)
	v_mul_f32_e32 v7, 0xbfb8aa3b, v210
	v_exp_f32_e32 v7, v7
	s_nop 0
	v_add_f32_e32 v7, 1.0, v7
	v_div_scale_f32 v8, s[8:9], v7, v7, v210
	v_rcp_f32_e32 v9, v8
	v_div_scale_f32 v10, vcc, v210, v7, v210
	v_fma_f32 v11, -v8, v9, 1.0
	v_fmac_f32_e32 v9, v11, v9
	v_mul_f32_e32 v11, v10, v9
	v_fma_f32 v12, -v8, v11, v10
	v_fmac_f32_e32 v11, v12, v9
	v_fma_f32 v8, -v8, v11, v10
	v_div_fmas_f32 v8, v8, v9, v11
	v_div_fixup_f32 v6, v8, v7, v210
	ds_write_b32 v5, v6
	v_add_u32_e32 v5, 0x800, v5
	s_waitcnt vmcnt(4)
	v_mul_f32_e32 v7, 0xbfb8aa3b, v211
	v_exp_f32_e32 v7, v7
	s_nop 0
	v_add_f32_e32 v7, 1.0, v7
	v_div_scale_f32 v8, s[8:9], v7, v7, v211
	v_rcp_f32_e32 v9, v8
	v_div_scale_f32 v10, vcc, v211, v7, v211
	v_fma_f32 v11, -v8, v9, 1.0
	v_fmac_f32_e32 v9, v11, v9
	v_mul_f32_e32 v11, v10, v9
	v_fma_f32 v12, -v8, v11, v10
	v_fmac_f32_e32 v11, v12, v9
	v_fma_f32 v8, -v8, v11, v10
	v_div_fmas_f32 v8, v8, v9, v11
	v_div_fixup_f32 v6, v8, v7, v211
	ds_write_b32 v5, v6
	v_add_u32_e32 v5, 0x800, v5
	s_waitcnt vmcnt(3)
	v_mul_f32_e32 v7, 0xbfb8aa3b, v212
	v_exp_f32_e32 v7, v7
	s_nop 0
	v_add_f32_e32 v7, 1.0, v7
	v_div_scale_f32 v8, s[8:9], v7, v7, v212
	v_rcp_f32_e32 v9, v8
	v_div_scale_f32 v10, vcc, v212, v7, v212
	v_fma_f32 v11, -v8, v9, 1.0
	v_fmac_f32_e32 v9, v11, v9
	v_mul_f32_e32 v11, v10, v9
	v_fma_f32 v12, -v8, v11, v10
	v_fmac_f32_e32 v11, v12, v9
	v_fma_f32 v8, -v8, v11, v10
	v_div_fmas_f32 v8, v8, v9, v11
	v_div_fixup_f32 v6, v8, v7, v212
	ds_write_b32 v5, v6
	v_add_u32_e32 v5, 0x800, v5
	s_waitcnt vmcnt(2)
	v_mul_f32_e32 v7, 0xbfb8aa3b, v213
	v_exp_f32_e32 v7, v7
	s_nop 0
	v_add_f32_e32 v7, 1.0, v7
	v_div_scale_f32 v8, s[8:9], v7, v7, v213
	v_rcp_f32_e32 v9, v8
	v_div_scale_f32 v10, vcc, v213, v7, v213
	v_fma_f32 v11, -v8, v9, 1.0
	v_fmac_f32_e32 v9, v11, v9
	v_mul_f32_e32 v11, v10, v9
	v_fma_f32 v12, -v8, v11, v10
	v_fmac_f32_e32 v11, v12, v9
	v_fma_f32 v8, -v8, v11, v10
	v_div_fmas_f32 v8, v8, v9, v11
	v_div_fixup_f32 v6, v8, v7, v213
	ds_write_b32 v5, v6
	v_add_u32_e32 v5, 0x800, v5
	s_waitcnt vmcnt(1)
	v_mul_f32_e32 v7, 0xbfb8aa3b, v214
	v_exp_f32_e32 v7, v7
	s_nop 0
	v_add_f32_e32 v7, 1.0, v7
	v_div_scale_f32 v8, s[8:9], v7, v7, v214
	v_rcp_f32_e32 v9, v8
	v_div_scale_f32 v10, vcc, v214, v7, v214
	v_fma_f32 v11, -v8, v9, 1.0
	v_fmac_f32_e32 v9, v11, v9
	v_mul_f32_e32 v11, v10, v9
	v_fma_f32 v12, -v8, v11, v10
	v_fmac_f32_e32 v11, v12, v9
	v_fma_f32 v8, -v8, v11, v10
	v_div_fmas_f32 v8, v8, v9, v11
	v_div_fixup_f32 v6, v8, v7, v214
	ds_write_b32 v5, v6
	v_add_u32_e32 v5, 0x800, v5
	s_waitcnt vmcnt(0)
	v_mul_f32_e32 v7, 0xbfb8aa3b, v215
	v_exp_f32_e32 v7, v7
	s_nop 0
	v_add_f32_e32 v7, 1.0, v7
	v_div_scale_f32 v8, s[8:9], v7, v7, v215
	v_rcp_f32_e32 v9, v8
	v_div_scale_f32 v10, vcc, v215, v7, v215
	v_fma_f32 v11, -v8, v9, 1.0
	v_fmac_f32_e32 v9, v11, v9
	v_mul_f32_e32 v11, v10, v9
	v_fma_f32 v12, -v8, v11, v10
	v_fmac_f32_e32 v11, v12, v9
	v_fma_f32 v8, -v8, v11, v10
	v_div_fmas_f32 v8, v8, v9, v11
	v_div_fixup_f32 v6, v8, v7, v215
	ds_write_b32 v5, v6
	v_add_u32_e32 v5, 0x800, v5
